# mixer C (differential attention): one static s_setprio 1 for waves 4-7 at unit start, reset at phase end
# speedup vs baseline: 1.0080x; 1.0070x over previous
.LBB0_753:
	v_mov_b32_e32 v244, v0
	s_nop 0
	v_readfirstlane_b32 s4, v244
	s_ashr_i32 s11, s4, 6
	s_cmp_gt_i32 s11, 3
	s_cselect_b64 s[12:13], -1, 0
	s_cbranch_scc0 .Lc_prio_done
	s_setprio 1
.Lc_prio_done:
	v_and_b32_e32 v245, 63, v244
	s_mov_b64 s[4:5], -1
	s_and_b64 vcc, exec, s[12:13]
	s_cbranch_vccz .LBB0_755
	v_mul_u32_u24_e32 v18, 0x2100, v245
	s_mov_b64 s[4:5], 0

.LBB0_797:
	s_setprio 0
	s_waitcnt vmcnt(0)
	s_barrier
	s_mov_b64 s[2:3], exec
	v_readlane_b32 s4, v255, 6
	v_readlane_b32 s5, v255, 7
	s_and_b64 s[4:5], s[2:3], s[4:5]
	s_movk_i32 s27, 0x7fff
	s_mov_b32 s36, 0xbfb8aa3b
	v_readlane_b32 s46, v255, 24
	v_readlane_b32 s47, v255, 25
	s_mov_b64 exec, s[4:5]
	s_cbranch_execz .Lcvt_site_5
	v_readlane_b32 s4, v255, 4
	v_readlane_b32 s5, v255, 5
	s_mov_b32 s20, s81
	v_mov_b32_e32 v2, s46
	s_waitcnt vmcnt(0) expcnt(0) lgkmcnt(0)
	ds_read_b32 v4, v2
	v_mov_b32_e32 v2, s47
	ds_read_b32 v2, v2
	s_waitcnt lgkmcnt(1)
	v_cmp_ne_u32_e32 vcc, 0, v4
	s_cbranch_vccnz .LBB0_813
	v_readlane_b32 s6, v255, 0
	v_readlane_b32 s7, v255, 1
	s_load_dwordx2 s[10:11], s[6:7], 0x4
	s_add_u32 s6, s4, 0x1000
	s_addc_u32 s7, s5, 0
	s_add_u32 s8, s4, 0x1100
	s_addc_u32 s9, s5, 0
	s_waitcnt lgkmcnt(0)
	s_mul_i32 s21, s10, s92
	s_add_u32 s10, s4, 0x1200
	s_mul_i32 s21, s21, s11
	s_addc_u32 s11, s5, 0
	s_add_u32 s12, s4, 0x1300
	s_addc_u32 s13, s5, 0
	s_mov_b32 s22, 1
	s_branch .LBB0_801
